# P0: the four-trip w_in gate-column staging loop issues its eight loads together
# speedup vs baseline: 1.0124x; 1.0019x over previous
.LBB0_95:
	s_mov_b64 s[4:5], 0x1a04000
	v_lshl_add_u64 v[12:13], v[0:1], 0, s[48:49]
	global_load_dwordx4 v[4:7], v[12:13], off
	global_load_dwordx4 v[8:11], v[12:13], off offset:16
	v_lshl_add_u64 v[12:13], v[12:13], 0, s[4:5]
	global_load_dwordx4 v[16:19], v[12:13], off
	global_load_dwordx4 v[20:23], v[12:13], off offset:16
	v_lshl_add_u64 v[12:13], v[12:13], 0, s[4:5]
	global_load_dwordx4 v[24:27], v[12:13], off
	global_load_dwordx4 v[28:31], v[12:13], off offset:16
	v_lshl_add_u64 v[12:13], v[12:13], 0, s[4:5]
	global_load_dwordx4 v[32:35], v[12:13], off
	global_load_dwordx4 v[36:39], v[12:13], off offset:16
	v_and_b32_e32 v12, 0x3ffffe00, v131
	v_and_b32_e32 v13, 0x100, v2
	v_lshlrev_b32_e32 v14, 1, v131
	v_lshlrev_b32_e32 v12, 2, v12
	v_lshlrev_b32_e32 v13, 2, v13
	v_and_b32_e32 v14, 0x3f0, v14
	v_add3_u32 v12, s25, v12, v13
	v_add_u32_e32 v2, 0x8000, v2
	v_add_u32_e32 v131, 0x200, v131
	v_add3_u32 v12, v12, v14, v3
	s_waitcnt vmcnt(7)
	ds_write2st64_b32 v12, v4, v5 offset1:32
	ds_write2st64_b32 v12, v6, v7 offset0:64 offset1:96
	s_waitcnt vmcnt(6)
	ds_write2st64_b32 v12, v8, v9 offset0:128 offset1:160
	ds_write2st64_b32 v12, v10, v11 offset0:192 offset1:224
	v_and_b32_e32 v12, 0x3ffffe00, v131
	v_and_b32_e32 v13, 0x100, v2
	v_lshlrev_b32_e32 v14, 1, v131
	v_lshlrev_b32_e32 v12, 2, v12
	v_lshlrev_b32_e32 v13, 2, v13
	v_and_b32_e32 v14, 0x3f0, v14
	v_add3_u32 v12, s25, v12, v13
	v_add_u32_e32 v2, 0x8000, v2
	v_add_u32_e32 v131, 0x200, v131
	v_add3_u32 v12, v12, v14, v3
	s_waitcnt vmcnt(5)
	ds_write2st64_b32 v12, v16, v17 offset1:32
	ds_write2st64_b32 v12, v18, v19 offset0:64 offset1:96
	s_waitcnt vmcnt(4)
	ds_write2st64_b32 v12, v20, v21 offset0:128 offset1:160
	ds_write2st64_b32 v12, v22, v23 offset0:192 offset1:224
	v_and_b32_e32 v12, 0x3ffffe00, v131
	v_and_b32_e32 v13, 0x100, v2
	v_lshlrev_b32_e32 v14, 1, v131
	v_lshlrev_b32_e32 v12, 2, v12
	v_lshlrev_b32_e32 v13, 2, v13
	v_and_b32_e32 v14, 0x3f0, v14
	v_add3_u32 v12, s25, v12, v13
	v_add_u32_e32 v2, 0x8000, v2
	v_add_u32_e32 v131, 0x200, v131
	v_add3_u32 v12, v12, v14, v3
	s_waitcnt vmcnt(3)
	ds_write2st64_b32 v12, v24, v25 offset1:32
	ds_write2st64_b32 v12, v26, v27 offset0:64 offset1:96
	s_waitcnt vmcnt(2)
	ds_write2st64_b32 v12, v28, v29 offset0:128 offset1:160
	ds_write2st64_b32 v12, v30, v31 offset0:192 offset1:224
	v_and_b32_e32 v12, 0x3ffffe00, v131
	v_and_b32_e32 v13, 0x100, v2
	v_lshlrev_b32_e32 v14, 1, v131
	v_lshlrev_b32_e32 v12, 2, v12
	v_lshlrev_b32_e32 v13, 2, v13
	v_and_b32_e32 v14, 0x3f0, v14
	v_add3_u32 v12, s25, v12, v13
	v_add_u32_e32 v2, 0x8000, v2
	v_add_u32_e32 v131, 0x200, v131
	v_add3_u32 v12, v12, v14, v3
	s_waitcnt vmcnt(1)
	ds_write2st64_b32 v12, v32, v33 offset1:32
	ds_write2st64_b32 v12, v34, v35 offset0:64 offset1:96
	s_waitcnt vmcnt(0)
	ds_write2st64_b32 v12, v36, v37 offset0:128 offset1:160
	ds_write2st64_b32 v12, v38, v39 offset0:192 offset1:224
